# each XCD (blockIdx mod 8) sweeps its own contiguous eighth of the matrix with a 32-row band, instead of all XCDs sharing one 250-row band
# baseline (speedup 1.0000x reference)
_Z11attn_kernelPKfS0_PKDv8_DF16_S0_Pfi:
	s_load_dwordx2 s[28:29], s[0:1], 0x0
	v_cmp_gt_u32_e32 vcc, 16, v0
	s_and_saveexec_b64 s[4:5], vcc
	v_lshlrev_b32_e32 v1, 2, v0
	v_mov_b32_e32 v2, 0
	ds_write_b32 v1, v2 offset:36864
	s_or_b64 exec, exec, s[4:5]
	s_load_dword s33, s[0:1], 0x28
	v_bfe_u32 v1, v0, 6, 2
	v_lshl_or_b32 v82, s2, 2, v1
	v_readfirstlane_b32 s34, v0
	s_cmp_gt_u32 s34, 0xff
	s_cbranch_scc1 .Lsc_early_skip
	v_and_b32_e32 v3, 63, v0
	v_lshlrev_b32_e32 v2, 4, v3
	s_lshr_b32 s55, s34, 6
	s_mul_i32 s43, s55, 0x2800
	s_and_b32 s56, s2, 7
	s_lshr_b32 s57, s2, 3
	s_min_u32 s40, s56, 2
	s_mul_i32 s37, s56, 0x4d8
	s_mul_i32 s40, s40, 40
	s_add_u32 s37, s37, s40
	s_add_u32 s37, s37, s57
	s_and_b32 s47, s37, 1
	s_lshl_b32 s47, s47, 2
	s_mul_i32 s38, s37, 0x9c40
	s_lshl_b32 s40, s47, 4
	s_sub_u32 s38, s38, s40
	s_add_u32 s38, s38, s43
	s_waitcnt lgkmcnt(0)
	s_and_b32 s29, s29, 0xffff
	s_mov_b32 s30, 0x17d78400
	s_mov_b32 s31, 0x20000
	v_mov_b32_e32 v12, v2
	v_mov_b32_e32 v4, v2
	s_cmp_lg_u32 s55, 0
	s_cbranch_scc1 .Lsc_flpa
	v_max_u32_e32 v12, s47, v3
	v_lshlrev_b32_e32 v12, 4, v12

.Lsc_early_skip:
	s_waitcnt lgkmcnt(0)
	s_barrier
	v_cmp_gt_i32_e32 vcc, s33, v82
	s_and_saveexec_b64 s[4:5], vcc
	s_cbranch_execz .LBB1_384
	s_abs_i32 s3, s33
	v_cvt_f32_u32_e32 v2, s3
	s_movk_i32 s4, 0xff
	v_sub_u32_e32 v3, 0x270f, v82
	v_cmp_lt_u32_e32 vcc, s4, v0
	v_rcp_iflag_f32_e32 v2, v2
	v_sub_u32_e32 v5, 0, v3
	s_sub_i32 s4, 0, s3
	v_xor_b32_e32 v4, s33, v3
	v_mul_f32_e32 v2, 0x4f7ffffe, v2
	v_cvt_u32_f32_e32 v2, v2
	v_max_i32_e32 v3, v3, v5
	v_ashrrev_i32_e32 v4, 31, v4
	v_mul_lo_u32 v5, s4, v2
	v_mul_hi_u32 v5, v2, v5
	v_add_u32_e32 v2, v2, v5
	v_mul_hi_u32 v2, v3, v2
	v_mul_lo_u32 v5, v2, s3
	v_sub_u32_e32 v3, v3, v5
	v_add_u32_e32 v5, 1, v2
	v_cmp_le_u32_e64 s[4:5], s3, v3
	v_and_b32_e32 v83, 63, v0
	s_nop 0
	v_cndmask_b32_e64 v2, v2, v5, s[4:5]
	v_subrev_u32_e32 v5, s3, v3
	v_cndmask_b32_e64 v3, v3, v5, s[4:5]
	v_add_u32_e32 v5, 1, v2
	v_cmp_le_u32_e64 s[4:5], s3, v3
	s_nop 1
	v_cndmask_b32_e64 v2, v2, v5, s[4:5]
	v_xor_b32_e32 v2, v2, v4
	v_sub_u32_e32 v84, v2, v4
	s_and_saveexec_b64 s[4:5], vcc
	s_xor_b64 s[30:31], exec, s[4:5]
	s_cbranch_execz .LBB1_217
	v_cmp_lt_i32_e32 vcc, -1, v84
	s_and_saveexec_b64 s[34:35], vcc
	s_cbranch_execz .LBB1_216
	s_load_dwordx8 s[20:27], s[0:1], 0x8
	v_and_b32_e32 v69, 15, v0
	v_mov_b32_e32 v0, 0x8000
	v_lshrrev_b32_e32 v67, 4, v83
	v_lshl_or_b32 v88, v1, 10, v0
	s_mul_i32 s3, s2, 0x2710
	v_mul_u32_u24_e32 v0, 0x9c4, v1
	v_lshl_or_b32 v89, v69, 2, v67
	v_add3_u32 v90, s3, v0, v83
	v_lshlrev_b32_e32 v0, 2, v1
	v_mov_b32_e32 v2, 0x9000
	v_lshl_or_b32 v91, s2, 4, v0
	v_lshlrev_b32_e32 v0, 3, v89
	v_mov_b32_e32 v32, 0
	v_lshl_or_b32 v65, v1, 3, v2
	v_or_b32_e32 v2, 0x1e00, v0
	v_mov_b32_e32 v3, v32
	s_waitcnt lgkmcnt(0)
	v_lshl_add_u64 v[34:35], s[20:21], 0, v[2:3]
	v_or_b32_e32 v2, 0x1c00, v0
	v_lshl_add_u64 v[36:37], s[20:21], 0, v[2:3]
	v_or_b32_e32 v2, 0x1a00, v0
	v_lshl_add_u64 v[38:39], s[20:21], 0, v[2:3]
	v_or_b32_e32 v2, 0x1800, v0
	v_lshl_add_u64 v[40:41], s[20:21], 0, v[2:3]
	v_or_b32_e32 v2, 0x1600, v0
	v_lshl_add_u64 v[42:43], s[20:21], 0, v[2:3]
	v_or_b32_e32 v2, 0x1400, v0
	v_lshlrev_b32_e32 v63, 12, v1
	v_lshl_add_u64 v[44:45], s[20:21], 0, v[2:3]
	v_or_b32_e32 v2, 0x1200, v0
	v_mov_b32_e32 v1, v32
	v_lshl_or_b32 v71, v83, 3, v63
	v_lshl_or_b32 v73, v67, 3, v63
	v_lshl_add_u64 v[46:47], s[20:21], 0, v[2:3]
	v_or_b32_e32 v2, 0x1000, v0
	v_lshl_add_u64 v[50:51], s[20:21], 0, v[0:1]
	v_mbcnt_lo_u32_b32 v0, -1, 0
	v_or_b32_e32 v75, 4, v67
	v_or_b32_e32 v77, 8, v67
	v_or_b32_e32 v78, 12, v67
	v_or_b32_e32 v79, 16, v67
	v_or_b32_e32 v80, 20, v67
	v_or_b32_e32 v81, 24, v67
	v_or_b32_e32 v85, 28, v67
	v_or_b32_e32 v86, 64, v83
	v_or_b32_e32 v87, 0x4000, v63
	v_cmp_lt_u32_e64 s[0:1], 15, v83
	s_mul_i32 s39, s33, 0x9c4
	s_lshl_b32 s48, s33, 2
	v_or_b32_e32 v92, 0x200, v71
	v_or_b32_e32 v93, 0x204, v71
	v_or_b32_e32 v94, 0x100, v73
	v_lshl_add_u64 v[48:49], s[20:21], 0, v[2:3]
	s_mov_b32 s51, 0
	s_mov_b64 s[36:37], 0
	s_movk_i32 s49, 0x81
	s_mov_b32 s50, 0xff800000
	s_mov_b32 s38, 0x38d1b717
	v_mov_b32_e32 v95, 0xff800000
	v_mbcnt_hi_u32_b32 v96, -1, v0
	v_mov_b32_e32 v136, 0
	v_mov_b32_e32 v137, 0
	v_mov_b32_e32 v138, 0
	v_mov_b32_e32 v139, 0
	v_mov_b32_e32 v140, 0
	v_mov_b32_e32 v141, 0
	v_mov_b32_e32 v142, 0
	v_mov_b32_e32 v143, 0
	v_mov_b32_e32 v144, 0
	v_mov_b32_e32 v145, 0
	v_mov_b32_e32 v146, 0
	v_mov_b32_e32 v147, 0
	v_mov_b32_e32 v148, 0
	v_mov_b32_e32 v149, 0
	v_mov_b32_e32 v150, 0
	v_mov_b32_e32 v151, 0
	v_mov_b32_e32 v152, 0
	v_mov_b32_e32 v153, 0
	v_mov_b32_e32 v154, 0
	v_mov_b32_e32 v155, 0
	v_mov_b32_e32 v156, 0
	v_mov_b32_e32 v157, 0
	v_mov_b32_e32 v158, 0
	v_mov_b32_e32 v159, 0
	v_mov_b32_e32 v160, 0
	v_mov_b32_e32 v161, 0
	v_mov_b32_e32 v162, 0
	v_mov_b32_e32 v163, 0
	v_mov_b32_e32 v164, 0
	v_mov_b32_e32 v165, 0
	v_mov_b32_e32 v166, 0
	v_mov_b32_e32 v167, 0
	v_mov_b32_e32 v168, 0
	v_mov_b32_e32 v169, 0
	v_mov_b32_e32 v170, 0
	v_mov_b32_e32 v171, 0
	v_mov_b32_e32 v172, 0
	v_mov_b32_e32 v173, 0
	v_mov_b32_e32 v174, 0
	v_mov_b32_e32 v175, 0
	v_mov_b32_e32 v176, 0
	v_mov_b32_e32 v177, 0
	v_mov_b32_e32 v178, 0
	v_mov_b32_e32 v179, 0
	v_mov_b32_e32 v180, 0
	v_mov_b32_e32 v181, 0
	v_mov_b32_e32 v182, 0
	v_mov_b32_e32 v183, 0
	v_mov_b32_e32 v184, 0
	v_mov_b32_e32 v185, 0
	v_mov_b32_e32 v186, 0
	v_mov_b32_e32 v187, 0
	v_mov_b32_e32 v188, 0
	v_mov_b32_e32 v189, 0
	v_mov_b32_e32 v190, 0
	v_mov_b32_e32 v191, 0
	v_mov_b32_e32 v192, 0
	v_mov_b32_e32 v193, 0
	v_mov_b32_e32 v194, 0
	v_mov_b32_e32 v195, 0
	v_mov_b32_e32 v196, 0
	v_mov_b32_e32 v197, 0
	v_mov_b32_e32 v198, 0
	v_mov_b32_e32 v199, 0
	v_readfirstlane_b32 s54, v63
	s_lshr_b32 s54, s54, 12
	s_and_b32 s56, s2, 7
	s_lshr_b32 s57, s2, 3
	s_min_u32 s5, s56, 2
	s_mul_i32 s4, s56, 0x4d8
	s_mul_i32 s5, s5, 40
	s_add_u32 s4, s4, s5
	s_add_u32 s4, s4, s57
	s_cmp_lt_u32 s56, 2
	s_cselect_b32 s5, 32, 31
	s_mul_i32 s56, s54, s5
	s_add_u32 s4, s4, s56
	s_lshl_b32 s33, s5, 2
	s_mul_i32 s39, s33, 0x9c4
	s_lshl_b32 s48, s33, 2
	v_mov_b32_e32 v82, s4
	v_mov_b32_e32 v87, 0x4000
	v_mov_b32_e32 v88, 0x8000
	v_mov_b32_e32 v65, 0x9030
	s_movk_i32 s3, 0x9c4
	v_mad_u32_u24 v90, v82, s3, v83
	v_lshlrev_b32_e32 v91, 2, v82
	s_branch .LBB1_9

.LBB1_217:
	s_andn2_saveexec_b64 s[0:1], s[30:31]
	s_cbranch_execz .LBB1_384
	v_readfirstlane_b32 s34, v1
	v_readfirstlane_b32 s36, v84
	v_and_b32_e32 v3, 63, v0
	v_lshlrev_b32_e32 v2, 4, v3
	s_cmp_lt_i32 s36, 0
	s_cbranch_scc1 .LBB1_384
	s_add_i32 s36, s36, 1
	s_lshl_b32 s36, s36, 2
	s_sub_i32 s36, s36, 1
	s_lshr_b32 s33, s33, 2
	s_mov_b32 s55, s34
	s_mul_i32 s43, s55, 0x2800
	s_and_b32 s56, s2, 7
	s_lshr_b32 s57, s2, 3
	s_min_u32 s40, s56, 2
	s_mul_i32 s37, s56, 0x4d8
	s_mul_i32 s40, s40, 40
	s_add_u32 s37, s37, s40
	s_add_u32 s37, s37, s57
	s_cmp_lt_u32 s56, 2
	s_cselect_b32 s33, 32, 31
	s_waitcnt lgkmcnt(0)
	s_and_b32 s29, s29, 0xffff
	s_mov_b32 s30, 0x17d78400
	s_mov_b32 s31, 0x20000
	s_mov_b32 s35, 0
	s_movk_i32 s7, 0x40
	s_mov_b32 s9, 0x7fffffff
	s_lshl_b32 s44, s34, 12
	s_add_u32 s44, s44, 0x4000
	s_lshl_b32 s45, s34, 10
	s_add_u32 s45, s45, 0x8000
	s_lshl_b32 s46, s34, 4
	s_add_u32 s46, s46, 0x9000
	s_and_b32 s47, s37, 1
	s_lshl_b32 s47, s47, 2
	s_mul_i32 s38, s37, 0x9c40
	s_lshl_b32 s40, s47, 4
	s_sub_u32 s38, s38, s40
	s_add_u32 s38, s38, s43
